# speedup vs baseline: 1.0044x; 1.0020x over previous
.Lca_loop:
	s_setprio 2
	s_barrier
	v_mfma_f32_16x16x32_f16 v[84:87], v[6:9], v[50:53], v[18:21]
	v_mfma_f32_16x16x32_f16 v[88:91], v[10:13], v[50:53], v[38:41]
	ds_read_b128 v[56:59], v75 offset:2048
	ds_read_b128 v[60:63], v75 offset:3072
	v_mfma_f32_16x16x32_f16 v[84:87], v[2:5], v[42:45], v[84:87]
	v_mfma_f32_16x16x32_f16 v[88:91], v[14:17], v[42:45], v[88:91]
	s_waitcnt lgkmcnt(1)
	v_mfma_f32_16x16x32_f16 v[84:87], v[30:33], v[56:59], v[84:87]
	v_mfma_f32_16x16x32_f16 v[88:91], v[22:25], v[56:59], v[88:91]
	s_waitcnt lgkmcnt(0)
	v_mfma_f32_16x16x32_f16 v[84:87], v[34:37], v[60:63], v[84:87]
	v_mfma_f32_16x16x32_f16 v[88:91], v[26:29], v[60:63], v[88:91]
	s_nop 7
	s_setprio 0
	v_exp_f32_e32 v94, v86
	v_exp_f32_e32 v95, v90
	v_exp_f32_e32 v96, v84
	v_exp_f32_e32 v97, v88
	v_exp_f32_e32 v98, v85
	v_exp_f32_e32 v99, v89
	v_pk_add_f32 v[100:101], v[94:95], 1.0 op_sel_hi:[1,0]
	v_pk_fma_f32 v[102:103], v[94:95], s[8:9], v[92:93] op_sel_hi:[1,0,0]
	v_pk_fma_f32 v[100:101], v[96:97], v[100:101], v[100:101]
	v_pk_fma_f32 v[104:105], v[100:101], v[98:99], v[100:101]
	v_rcp_f32_e32 v104, v104
	v_rcp_f32_e32 v105, v105
	v_pk_fma_f32 v[102:103], v[102:103], v[98:99], v[102:103]
	v_pk_fma_f32 v[102:103], v[64:65], v[100:101], v[102:103]
	v_exp_f32_e32 v106, v87
	v_pk_mul_f32 v[64:65], v[102:103], v[104:105]
	v_exp_f32_e32 v108, v64
	v_exp_f32_e32 v109, v65
	v_exp_f32_e32 v107, v91
	v_pk_add_f32 v[110:111], v[108:109], 1.0 op_sel_hi:[1,0]
	v_pk_fma_f32 v[110:111], v[110:111], v[106:107], v[110:111]
	v_rcp_f32_e32 v110, v110
	v_rcp_f32_e32 v111, v111
	v_pk_add_f32 v[112:113], v[108:109], -1.0 op_sel_hi:[1,0]
	v_pk_mul_f32 v[112:113], v[112:113], v[110:111]
	v_cvt_pk_f16_f32 v114, v112, v113
	ds_write_b32 v81, v114 offset:0
	s_waitcnt lgkmcnt(0)
	v_min_f32_e32 v64, 0x42700000, v64
	v_min_f32_e32 v65, 0x42700000, v65
	v_readfirstlane_b32 s10, v67
	v_readfirstlane_b32 s11, v68
	global_load_dword v67, v66, s[0:1] sc1
	global_load_dword v68, v66, s[0:1] offset:4 sc1
	s_min_u32 s10, s10, s11
	s_max_u32 s14, s14, s10
	s_add_u32 s13, s12, 3
	s_min_u32 s13, s13, 450
	s_cmp_ge_u32 s14, s13
	s_cbranch_scc0 .Lca_slow_9
